# gather address computed with one v_lshl_or_b32 (column-index mask removed, as in the baseline)
# baseline (speedup 1.0000x reference)
.Lhq0_s0_top:
	v_sub_u32_e32 v2, v5, v46
	ds_read_b64 v[6:7], v46
	ds_read_b64 v[8:9], v46 offset:8
	ds_read_b64 v[10:11], v46 offset:16
	ds_read_b64 v[12:13], v46 offset:24
	v_cmp_lt_i32_e64 s[30:31], 0, v2
	s_and_b64 s[30:31], s[30:31], exec
	s_cbranch_scc0 .Lhq0_s0_done
	v_cmp_lt_i32_e64 s[32:33], 8, v2
	v_cmp_lt_i32_e64 s[34:35], 16, v2
	v_cmp_lt_i32_e64 s[36:37], 24, v2
	v_cmp_lt_i32_e64 s[42:43], 32, v2
	v_add_u32_e32 v46, 32, v46
	v_min_i32_e32 v46, v46, v5
	s_waitcnt lgkmcnt(0)
	s_mov_b64 exec, s[30:31]
	v_lshl_or_b32 v3, v6, 7, v1
	global_load_dwordx4 v[18:21], v3, s[8:9]
	s_and_b64 exec, s[32:33], s[32:33]
	s_cbranch_scc0 .Lhq0_s0_ld_done
	v_lshl_or_b32 v4, v8, 7, v1
	global_load_dwordx4 v[22:25], v4, s[8:9]
	s_and_b64 exec, s[34:35], s[34:35]
	s_cbranch_scc0 .Lhq0_s0_ld_done
	v_lshl_or_b32 v3, v10, 7, v1
	global_load_dwordx4 v[26:29], v3, s[8:9]
	s_and_b64 exec, s[36:37], s[36:37]
	s_cbranch_scc0 .Lhq0_s0_ld_done
	v_lshl_or_b32 v4, v12, 7, v1
	global_load_dwordx4 v[30:33], v4, s[8:9]

.Lhq0_s1_top:
	v_sub_u32_e32 v2, v5, v47
	ds_read_b64 v[6:7], v47
	ds_read_b64 v[8:9], v47 offset:8
	ds_read_b64 v[10:11], v47 offset:16
	ds_read_b64 v[12:13], v47 offset:24
	v_cmp_lt_i32_e64 s[30:31], 0, v2
	s_and_b64 s[30:31], s[30:31], exec
	s_cbranch_scc0 .Lhq0_s1_done
	v_cmp_lt_i32_e64 s[32:33], 8, v2
	v_cmp_lt_i32_e64 s[34:35], 16, v2
	v_cmp_lt_i32_e64 s[36:37], 24, v2
	v_cmp_lt_i32_e64 s[42:43], 32, v2
	v_add_u32_e32 v47, 32, v47
	v_min_i32_e32 v47, v47, v5
	s_waitcnt lgkmcnt(0)
	s_mov_b64 exec, s[30:31]
	v_lshl_or_b32 v3, v6, 7, v1
	global_load_dwordx4 v[18:21], v3, s[8:9]
	s_and_b64 exec, s[32:33], s[32:33]
	s_cbranch_scc0 .Lhq0_s1_ld_done
	v_lshl_or_b32 v4, v8, 7, v1
	global_load_dwordx4 v[22:25], v4, s[8:9]
	s_and_b64 exec, s[34:35], s[34:35]
	s_cbranch_scc0 .Lhq0_s1_ld_done
	v_lshl_or_b32 v3, v10, 7, v1
	global_load_dwordx4 v[26:29], v3, s[8:9]
	s_and_b64 exec, s[36:37], s[36:37]
	s_cbranch_scc0 .Lhq0_s1_ld_done
	v_lshl_or_b32 v4, v12, 7, v1
	global_load_dwordx4 v[30:33], v4, s[8:9]

.Lhq0_s2_top:
	v_sub_u32_e32 v2, v5, v48
	ds_read_b64 v[6:7], v48
	ds_read_b64 v[8:9], v48 offset:8
	ds_read_b64 v[10:11], v48 offset:16
	ds_read_b64 v[12:13], v48 offset:24
	v_cmp_lt_i32_e64 s[30:31], 0, v2
	s_and_b64 s[30:31], s[30:31], exec
	s_cbranch_scc0 .Lhq0_s2_done
	v_cmp_lt_i32_e64 s[32:33], 8, v2
	v_cmp_lt_i32_e64 s[34:35], 16, v2
	v_cmp_lt_i32_e64 s[36:37], 24, v2
	v_cmp_lt_i32_e64 s[42:43], 32, v2
	v_add_u32_e32 v48, 32, v48
	v_min_i32_e32 v48, v48, v5
	s_waitcnt lgkmcnt(0)
	s_mov_b64 exec, s[30:31]
	v_lshl_or_b32 v3, v6, 7, v1
	global_load_dwordx4 v[18:21], v3, s[8:9]
	s_and_b64 exec, s[32:33], s[32:33]
	s_cbranch_scc0 .Lhq0_s2_ld_done
	v_lshl_or_b32 v4, v8, 7, v1
	global_load_dwordx4 v[22:25], v4, s[8:9]
	s_and_b64 exec, s[34:35], s[34:35]
	s_cbranch_scc0 .Lhq0_s2_ld_done
	v_lshl_or_b32 v3, v10, 7, v1
	global_load_dwordx4 v[26:29], v3, s[8:9]
	s_and_b64 exec, s[36:37], s[36:37]
	s_cbranch_scc0 .Lhq0_s2_ld_done
	v_lshl_or_b32 v4, v12, 7, v1
	global_load_dwordx4 v[30:33], v4, s[8:9]

.Lhq0_s3_top:
	v_sub_u32_e32 v2, v5, v49
	ds_read_b64 v[6:7], v49
	ds_read_b64 v[8:9], v49 offset:8
	ds_read_b64 v[10:11], v49 offset:16
	ds_read_b64 v[12:13], v49 offset:24
	v_cmp_lt_i32_e64 s[30:31], 0, v2
	s_and_b64 s[30:31], s[30:31], exec
	s_cbranch_scc0 .Lhq0_s3_done
	v_cmp_lt_i32_e64 s[32:33], 8, v2
	v_cmp_lt_i32_e64 s[34:35], 16, v2
	v_cmp_lt_i32_e64 s[36:37], 24, v2
	v_cmp_lt_i32_e64 s[42:43], 32, v2
	v_add_u32_e32 v49, 32, v49
	v_min_i32_e32 v49, v49, v5
	s_waitcnt lgkmcnt(0)
	s_mov_b64 exec, s[30:31]
	v_lshl_or_b32 v3, v6, 7, v1
	global_load_dwordx4 v[18:21], v3, s[8:9]
	s_and_b64 exec, s[32:33], s[32:33]
	s_cbranch_scc0 .Lhq0_s3_ld_done
	v_lshl_or_b32 v4, v8, 7, v1
	global_load_dwordx4 v[22:25], v4, s[8:9]
	s_and_b64 exec, s[34:35], s[34:35]
	s_cbranch_scc0 .Lhq0_s3_ld_done
	v_lshl_or_b32 v3, v10, 7, v1
	global_load_dwordx4 v[26:29], v3, s[8:9]
	s_and_b64 exec, s[36:37], s[36:37]
	s_cbranch_scc0 .Lhq0_s3_ld_done
	v_lshl_or_b32 v4, v12, 7, v1
	global_load_dwordx4 v[30:33], v4, s[8:9]

.Lhq0_s4_top:
	v_sub_u32_e32 v2, v5, v50
	ds_read_b64 v[6:7], v50
	ds_read_b64 v[8:9], v50 offset:8
	ds_read_b64 v[10:11], v50 offset:16
	ds_read_b64 v[12:13], v50 offset:24
	v_cmp_lt_i32_e64 s[30:31], 0, v2
	s_and_b64 s[30:31], s[30:31], exec
	s_cbranch_scc0 .Lhq0_s4_done
	v_cmp_lt_i32_e64 s[32:33], 8, v2
	v_cmp_lt_i32_e64 s[34:35], 16, v2
	v_cmp_lt_i32_e64 s[36:37], 24, v2
	v_cmp_lt_i32_e64 s[42:43], 32, v2
	v_add_u32_e32 v50, 32, v50
	v_min_i32_e32 v50, v50, v5
	s_waitcnt lgkmcnt(0)
	s_mov_b64 exec, s[30:31]
	v_lshl_or_b32 v3, v6, 7, v1
	global_load_dwordx4 v[18:21], v3, s[8:9]
	s_and_b64 exec, s[32:33], s[32:33]
	s_cbranch_scc0 .Lhq0_s4_ld_done
	v_lshl_or_b32 v4, v8, 7, v1
	global_load_dwordx4 v[22:25], v4, s[8:9]
	s_and_b64 exec, s[34:35], s[34:35]
	s_cbranch_scc0 .Lhq0_s4_ld_done
	v_lshl_or_b32 v3, v10, 7, v1
	global_load_dwordx4 v[26:29], v3, s[8:9]
	s_and_b64 exec, s[36:37], s[36:37]
	s_cbranch_scc0 .Lhq0_s4_ld_done
	v_lshl_or_b32 v4, v12, 7, v1
	global_load_dwordx4 v[30:33], v4, s[8:9]

.Lhq0_fb0_top:
	v_cmp_lt_i32_e32 vcc, v46, v51
	s_and_b64 exec, exec, vcc
	s_cbranch_scc0 .Lhq0_fb0_done
	v_lshlrev_b32_e32 v3, 3, v46
	global_load_dwordx2 v[6:7], v3, s[6:7]
	v_add_u32_e32 v46, 1, v46
	s_waitcnt vmcnt(0)
	v_lshl_or_b32 v4, v6, 7, v1
	global_load_dwordx4 v[18:21], v4, s[8:9]
	s_waitcnt vmcnt(0)
	v_cvt_f32_f16_e32 v42, v18
	v_cvt_f32_f16_sdwa v43, v18 dst_sel:DWORD dst_unused:UNUSED_PAD src0_sel:WORD_1
	v_cvt_f32_f16_e32 v44, v20
	v_cvt_f32_f16_sdwa v45, v20 dst_sel:DWORD dst_unused:UNUSED_PAD src0_sel:WORD_1
	v_cvt_f32_f16_e32 v18, v19
	v_cvt_f32_f16_sdwa v19, v19 dst_sel:DWORD dst_unused:UNUSED_PAD src0_sel:WORD_1
	v_cvt_f32_f16_e32 v20, v21
	v_cvt_f32_f16_sdwa v21, v21 dst_sel:DWORD dst_unused:UNUSED_PAD src0_sel:WORD_1
	v_fma_f32 v56, v7, v42, v56
	v_fma_f32 v57, v7, v43, v57
	v_fma_f32 v58, v7, v18, v58
	v_fma_f32 v59, v7, v19, v59
	v_fma_f32 v60, v7, v44, v60
	v_fma_f32 v61, v7, v45, v61
	v_fma_f32 v62, v7, v20, v62
	v_fma_f32 v63, v7, v21, v63
	s_branch .Lhq0_fb0_top

.Lhq0_fb1_top:
	v_cmp_lt_i32_e32 vcc, v47, v52
	s_and_b64 exec, exec, vcc
	s_cbranch_scc0 .Lhq0_fb1_done
	v_lshlrev_b32_e32 v3, 3, v47
	global_load_dwordx2 v[6:7], v3, s[6:7]
	v_add_u32_e32 v47, 1, v47
	s_waitcnt vmcnt(0)
	v_lshl_or_b32 v4, v6, 7, v1
	global_load_dwordx4 v[18:21], v4, s[8:9]
	s_waitcnt vmcnt(0)
	v_cvt_f32_f16_e32 v42, v18
	v_cvt_f32_f16_sdwa v43, v18 dst_sel:DWORD dst_unused:UNUSED_PAD src0_sel:WORD_1
	v_cvt_f32_f16_e32 v44, v20
	v_cvt_f32_f16_sdwa v45, v20 dst_sel:DWORD dst_unused:UNUSED_PAD src0_sel:WORD_1
	v_cvt_f32_f16_e32 v18, v19
	v_cvt_f32_f16_sdwa v19, v19 dst_sel:DWORD dst_unused:UNUSED_PAD src0_sel:WORD_1
	v_cvt_f32_f16_e32 v20, v21
	v_cvt_f32_f16_sdwa v21, v21 dst_sel:DWORD dst_unused:UNUSED_PAD src0_sel:WORD_1
	v_fma_f32 v64, v7, v42, v64
	v_fma_f32 v65, v7, v43, v65
	v_fma_f32 v66, v7, v18, v66
	v_fma_f32 v67, v7, v19, v67
	v_fma_f32 v68, v7, v44, v68
	v_fma_f32 v69, v7, v45, v69
	v_fma_f32 v70, v7, v20, v70
	v_fma_f32 v71, v7, v21, v71
	s_branch .Lhq0_fb1_top

.Lhq0_fb2_top:
	v_cmp_lt_i32_e32 vcc, v48, v53
	s_and_b64 exec, exec, vcc
	s_cbranch_scc0 .Lhq0_fb2_done
	v_lshlrev_b32_e32 v3, 3, v48
	global_load_dwordx2 v[6:7], v3, s[6:7]
	v_add_u32_e32 v48, 1, v48
	s_waitcnt vmcnt(0)
	v_lshl_or_b32 v4, v6, 7, v1
	global_load_dwordx4 v[18:21], v4, s[8:9]
	s_waitcnt vmcnt(0)
	v_cvt_f32_f16_e32 v42, v18
	v_cvt_f32_f16_sdwa v43, v18 dst_sel:DWORD dst_unused:UNUSED_PAD src0_sel:WORD_1
	v_cvt_f32_f16_e32 v44, v20
	v_cvt_f32_f16_sdwa v45, v20 dst_sel:DWORD dst_unused:UNUSED_PAD src0_sel:WORD_1
	v_cvt_f32_f16_e32 v18, v19
	v_cvt_f32_f16_sdwa v19, v19 dst_sel:DWORD dst_unused:UNUSED_PAD src0_sel:WORD_1
	v_cvt_f32_f16_e32 v20, v21
	v_cvt_f32_f16_sdwa v21, v21 dst_sel:DWORD dst_unused:UNUSED_PAD src0_sel:WORD_1
	v_fma_f32 v72, v7, v42, v72
	v_fma_f32 v73, v7, v43, v73
	v_fma_f32 v74, v7, v18, v74
	v_fma_f32 v75, v7, v19, v75
	v_fma_f32 v76, v7, v44, v76
	v_fma_f32 v77, v7, v45, v77
	v_fma_f32 v78, v7, v20, v78
	v_fma_f32 v79, v7, v21, v79
	s_branch .Lhq0_fb2_top

.Lhq0_fb3_top:
	v_cmp_lt_i32_e32 vcc, v49, v54
	s_and_b64 exec, exec, vcc
	s_cbranch_scc0 .Lhq0_fb3_done
	v_lshlrev_b32_e32 v3, 3, v49
	global_load_dwordx2 v[6:7], v3, s[6:7]
	v_add_u32_e32 v49, 1, v49
	s_waitcnt vmcnt(0)
	v_lshl_or_b32 v4, v6, 7, v1
	global_load_dwordx4 v[18:21], v4, s[8:9]
	s_waitcnt vmcnt(0)
	v_cvt_f32_f16_e32 v42, v18
	v_cvt_f32_f16_sdwa v43, v18 dst_sel:DWORD dst_unused:UNUSED_PAD src0_sel:WORD_1
	v_cvt_f32_f16_e32 v44, v20
	v_cvt_f32_f16_sdwa v45, v20 dst_sel:DWORD dst_unused:UNUSED_PAD src0_sel:WORD_1
	v_cvt_f32_f16_e32 v18, v19
	v_cvt_f32_f16_sdwa v19, v19 dst_sel:DWORD dst_unused:UNUSED_PAD src0_sel:WORD_1
	v_cvt_f32_f16_e32 v20, v21
	v_cvt_f32_f16_sdwa v21, v21 dst_sel:DWORD dst_unused:UNUSED_PAD src0_sel:WORD_1
	v_fma_f32 v80, v7, v42, v80
	v_fma_f32 v81, v7, v43, v81
	v_fma_f32 v82, v7, v18, v82
	v_fma_f32 v83, v7, v19, v83
	v_fma_f32 v84, v7, v44, v84
	v_fma_f32 v85, v7, v45, v85
	v_fma_f32 v86, v7, v20, v86
	v_fma_f32 v87, v7, v21, v87
	s_branch .Lhq0_fb3_top

.Lhq0_fb4_top:
	v_cmp_lt_i32_e32 vcc, v50, v55
	s_and_b64 exec, exec, vcc
	s_cbranch_scc0 .Lhq0_fb4_done
	v_lshlrev_b32_e32 v3, 3, v50
	global_load_dwordx2 v[6:7], v3, s[6:7]
	v_add_u32_e32 v50, 1, v50
	s_waitcnt vmcnt(0)
	v_lshl_or_b32 v4, v6, 7, v1
	global_load_dwordx4 v[18:21], v4, s[8:9]
	s_waitcnt vmcnt(0)
	v_cvt_f32_f16_e32 v42, v18
	v_cvt_f32_f16_sdwa v43, v18 dst_sel:DWORD dst_unused:UNUSED_PAD src0_sel:WORD_1
	v_cvt_f32_f16_e32 v44, v20
	v_cvt_f32_f16_sdwa v45, v20 dst_sel:DWORD dst_unused:UNUSED_PAD src0_sel:WORD_1
	v_cvt_f32_f16_e32 v18, v19
	v_cvt_f32_f16_sdwa v19, v19 dst_sel:DWORD dst_unused:UNUSED_PAD src0_sel:WORD_1
	v_cvt_f32_f16_e32 v20, v21
	v_cvt_f32_f16_sdwa v21, v21 dst_sel:DWORD dst_unused:UNUSED_PAD src0_sel:WORD_1
	v_fma_f32 v88, v7, v42, v88
	v_fma_f32 v89, v7, v43, v89
	v_fma_f32 v90, v7, v18, v90
	v_fma_f32 v91, v7, v19, v91
	v_fma_f32 v92, v7, v44, v92
	v_fma_f32 v93, v7, v45, v93
	v_fma_f32 v94, v7, v20, v94
	v_fma_f32 v95, v7, v21, v95
	s_branch .Lhq0_fb4_top
